# v23 + hand-scheduled MoE up-projection tile epilogue (power-of-two scalings folded into constants, 8-element batches, 185 fewer instructions per tile and wave; bit-identical results)
# speedup vs baseline: 1.0042x; 1.0042x over previous
.LBB0_1060:
	s_add_u32 s4, s26, 0x100
	s_addc_u32 s5, s27, 0
	s_add_u32 s54, s50, s26
	s_addc_u32 s55, s51, s27
	s_cmp_eq_u32 s52, 12
	s_cselect_b64 vcc, -1, 0
	s_and_b64 s[24:25], vcc, exec
	s_cselect_b32 s53, 0, s4
	s_cselect_b32 s25, s21, s55
	s_cselect_b32 s24, s49, s54
	v_lshl_add_u64 v[18:19], v[186:187], 0, s[26:27]
	s_add_i32 m0, s33, 0xc000
	ds_read_b128 v[210:213], v203
	ds_read_b128 v[214:217], v203 offset:1024
	ds_read_b128 v[218:221], v203 offset:2048
	ds_read_b128 v[222:225], v203 offset:3072
	ds_read_b128 v[226:229], v203 offset:4096
	ds_read_b128 v[230:233], v203 offset:5120
	ds_read_b128 v[234:237], v203 offset:6144
	ds_read_b128 v[238:241], v203 offset:7168
	global_load_lds_dwordx4 v[18:19], off
	v_lshl_add_u64 v[18:19], v[184:185], 0, s[26:27]
	s_add_i32 m0, s33, 0xe000
	s_nop 0
	global_load_lds_dwordx4 v[18:19], off
	s_waitcnt lgkmcnt(8)
	s_barrier
	s_waitcnt lgkmcnt(0)
	s_waitcnt lgkmcnt(0)
	v_mfma_f32_16x16x128_f8f6f4 v[158:161], v[2:9], v[210:217], v[158:161]
	v_mfma_f32_16x16x128_f8f6f4 v[150:153], v[10:17], v[210:217], v[150:153]
	v_mfma_f32_16x16x128_f8f6f4 v[142:145], v[2:9], v[218:225], v[142:145]
	v_mfma_f32_16x16x128_f8f6f4 v[134:137], v[10:17], v[218:225], v[134:137]
	v_mfma_f32_16x16x128_f8f6f4 v[126:129], v[2:9], v[226:233], v[126:129]
	v_mfma_f32_16x16x128_f8f6f4 v[118:121], v[10:17], v[226:233], v[118:121]
	v_mfma_f32_16x16x128_f8f6f4 v[110:113], v[2:9], v[234:241], v[110:113]
	v_mfma_f32_16x16x128_f8f6f4 v[102:105], v[10:17], v[234:241], v[102:105]
	s_barrier
	s_add_i32 s26, s39, s23
	v_add_u32_e32 v30, s40, v201
	v_lshl_add_u64 v[188:189], s[24:25], 0, v[164:165]
	s_mov_b32 m0, s26
	ds_read_b128 v[18:21], v30
	ds_read_b128 v[22:25], v30 offset:1024
	ds_read_b128 v[26:29], v30 offset:2048
	ds_read_b128 v[30:33], v30 offset:3072
	global_load_lds_dwordx4 v[188:189], off
	v_lshl_add_u64 v[190:191], s[24:25], 0, v[166:167]
	s_add_i32 m0, s26, 0x2000
	s_nop 0
	global_load_lds_dwordx4 v[190:191], off
	s_barrier
	s_waitcnt lgkmcnt(0)
	s_waitcnt lgkmcnt(0)
	v_mfma_f32_16x16x128_f8f6f4 v[154:157], v[18:25], v[210:217], v[154:157]
	v_mfma_f32_16x16x128_f8f6f4 v[146:149], v[26:33], v[210:217], v[146:149]
	v_mfma_f32_16x16x128_f8f6f4 v[138:141], v[18:25], v[218:225], v[138:141]
	v_mfma_f32_16x16x128_f8f6f4 v[130:133], v[26:33], v[218:225], v[130:133]
	v_mfma_f32_16x16x128_f8f6f4 v[122:125], v[18:25], v[226:233], v[122:125]
	v_mfma_f32_16x16x128_f8f6f4 v[114:117], v[26:33], v[226:233], v[114:117]
	v_mfma_f32_16x16x128_f8f6f4 v[106:109], v[18:25], v[234:241], v[106:109]
	v_mfma_f32_16x16x128_f8f6f4 v[98:101], v[26:33], v[234:241], v[98:101]
	s_add_u32 s26, s10, s53
	s_mov_b32 m0, s33
	s_addc_u32 s27, s11, 0
	v_cndmask_b32_e32 v162, v208, v206, vcc
	s_barrier
	ds_read_b128 v[210:213], v203 offset:16384
	ds_read_b128 v[214:217], v203 offset:17408
	ds_read_b128 v[218:221], v203 offset:18432
	ds_read_b128 v[222:225], v203 offset:19456
	ds_read_b128 v[226:229], v203 offset:20480
	ds_read_b128 v[230:233], v203 offset:21504
	ds_read_b128 v[234:237], v203 offset:22528
	ds_read_b128 v[238:241], v203 offset:23552
	v_cndmask_b32_e32 v192, v178, v207, vcc
	global_load_lds_dwordx4 v162, s[26:27]
	s_mov_b32 m0, s34
	v_mov_b32_e32 v193, v163
	global_load_lds_dwordx4 v192, s[26:27]
	s_waitcnt vmcnt(10)
	s_barrier
	s_waitcnt lgkmcnt(0)
	v_lshl_add_u64 v[194:195], s[26:27], 0, v[162:163]
	v_lshl_add_u64 v[192:193], s[26:27], 0, v[192:193]
	s_waitcnt lgkmcnt(0)
	v_mfma_f32_16x16x128_f8f6f4 v[94:97], v[2:9], v[210:217], v[94:97]
	v_mfma_f32_16x16x128_f8f6f4 v[86:89], v[10:17], v[210:217], v[86:89]
	v_mfma_f32_16x16x128_f8f6f4 v[78:81], v[2:9], v[218:225], v[78:81]
	v_mfma_f32_16x16x128_f8f6f4 v[70:73], v[10:17], v[218:225], v[70:73]
	v_mfma_f32_16x16x128_f8f6f4 v[62:65], v[2:9], v[226:233], v[62:65]
	v_mfma_f32_16x16x128_f8f6f4 v[54:57], v[10:17], v[226:233], v[54:57]
	v_mfma_f32_16x16x128_f8f6f4 v[46:49], v[2:9], v[234:241], v[46:49]
	v_mfma_f32_16x16x128_f8f6f4 v[38:41], v[10:17], v[234:241], v[38:41]
	s_barrier
	v_add_u32_e32 v14, 0x18000, v201
	ds_read_b128 v[2:5], v14
	ds_read_b128 v[6:9], v14 offset:1024
	ds_read_b128 v[10:13], v14 offset:2048
	ds_read_b128 v[14:17], v14 offset:3072
	s_add_u32 s54, s24, 0x40000
	s_addc_u32 s55, s25, 0
	s_add_i32 s53, s40, s23
	v_lshl_add_u64 v[242:243], s[54:55], 0, v[164:165]
	s_mov_b32 m0, s53
	s_nop 0
	global_load_lds_dwordx4 v[242:243], off
	v_lshl_add_u64 v[242:243], s[54:55], 0, v[166:167]
	s_add_i32 m0, s53, 0x2000
	s_nop 0
	global_load_lds_dwordx4 v[242:243], off
	s_waitcnt vmcnt(6)
	s_barrier
	v_mfma_f32_16x16x128_f8f6f4 v[90:93], v[18:25], v[210:217], v[90:93]
	v_mfma_f32_16x16x128_f8f6f4 v[82:85], v[26:33], v[210:217], v[82:85]
	v_mfma_f32_16x16x128_f8f6f4 v[74:77], v[18:25], v[218:225], v[74:77]
	v_mfma_f32_16x16x128_f8f6f4 v[66:69], v[26:33], v[218:225], v[66:69]
	v_mfma_f32_16x16x128_f8f6f4 v[58:61], v[18:25], v[226:233], v[58:61]
	v_mfma_f32_16x16x128_f8f6f4 v[50:53], v[26:33], v[226:233], v[50:53]
	v_mfma_f32_16x16x128_f8f6f4 v[42:45], v[18:25], v[234:241], v[42:45]
	v_mfma_f32_16x16x128_f8f6f4 v[34:37], v[26:33], v[234:241], v[34:37]
	s_add_i32 s53, 0, 0x18000
	s_barrier
	v_cndmask_b32_e32 v172, v180, v174, vcc
	s_mov_b32 m0, s35
	v_cndmask_b32_e32 v226, v182, v176, vcc
	v_mov_b32_e32 v227, v173
	v_lshl_add_u64 v[228:229], s[26:27], 0, v[172:173]
	ds_read_b128 v[18:21], v203 offset:32768
	ds_read_b128 v[22:25], v203 offset:33792
	ds_read_b128 v[26:29], v203 offset:34816
	ds_read_b128 v[30:33], v203 offset:35840
	ds_read_b128 v[210:213], v203 offset:36864
	ds_read_b128 v[214:217], v203 offset:37888
	ds_read_b128 v[218:221], v203 offset:38912
	ds_read_b128 v[222:225], v203 offset:39936
	global_load_lds_dwordx4 v[228:229], off
	v_lshl_add_u64 v[226:227], s[26:27], 0, v[226:227]
	s_mov_b32 m0, s36
	s_nop 0
	global_load_lds_dwordx4 v[226:227], off
	s_waitcnt lgkmcnt(8)
	s_barrier
	s_waitcnt lgkmcnt(0)
	s_waitcnt lgkmcnt(0)
	v_mfma_f32_16x16x128_f8f6f4 v[158:161], v[2:9], v[18:25], v[158:161]
	v_mfma_f32_16x16x128_f8f6f4 v[150:153], v[10:17], v[18:25], v[150:153]
	v_mfma_f32_16x16x128_f8f6f4 v[142:145], v[2:9], v[26:33], v[142:145]
	v_mfma_f32_16x16x128_f8f6f4 v[134:137], v[10:17], v[26:33], v[134:137]
	v_mfma_f32_16x16x128_f8f6f4 v[126:129], v[2:9], v[210:217], v[126:129]
	v_mfma_f32_16x16x128_f8f6f4 v[118:121], v[10:17], v[210:217], v[118:121]
	v_mfma_f32_16x16x128_f8f6f4 v[110:113], v[2:9], v[218:225], v[110:113]
	v_mfma_f32_16x16x128_f8f6f4 v[102:105], v[10:17], v[218:225], v[102:105]
	s_barrier
	s_add_i32 s26, 0, 0x1c000
	s_add_i32 s27, s53, s23
	v_add_u32_e32 v162, s26, v201
	v_lshl_add_u64 v[188:189], v[188:189], 0, s[16:17]
	s_mov_b32 m0, s27
	ds_read_b128 v[226:229], v162
	ds_read_b128 v[230:233], v162 offset:1024
	ds_read_b128 v[234:237], v162 offset:2048
	ds_read_b128 v[238:241], v162 offset:3072
	global_load_lds_dwordx4 v[188:189], off
	v_lshl_add_u64 v[188:189], v[190:191], 0, s[16:17]
	s_add_i32 m0, s27, 0x2000
	s_nop 0
	global_load_lds_dwordx4 v[188:189], off
	s_barrier
	s_waitcnt lgkmcnt(0)
	s_waitcnt lgkmcnt(0)
	v_mfma_f32_16x16x128_f8f6f4 v[154:157], v[226:233], v[18:25], v[154:157]
	v_mfma_f32_16x16x128_f8f6f4 v[146:149], v[234:241], v[18:25], v[146:149]
	v_mfma_f32_16x16x128_f8f6f4 v[138:141], v[226:233], v[26:33], v[138:141]
	v_mfma_f32_16x16x128_f8f6f4 v[130:133], v[234:241], v[26:33], v[130:133]
	v_mfma_f32_16x16x128_f8f6f4 v[122:125], v[226:233], v[210:217], v[122:125]
	v_mfma_f32_16x16x128_f8f6f4 v[114:117], v[234:241], v[210:217], v[114:117]
	v_mfma_f32_16x16x128_f8f6f4 v[106:109], v[226:233], v[218:225], v[106:109]
	v_mfma_f32_16x16x128_f8f6f4 v[98:101], v[234:241], v[218:225], v[98:101]
	s_mov_b32 m0, s37
	v_lshl_add_u64 v[188:189], v[194:195], 0, s[16:17]
	s_barrier
	ds_read_b128 v[18:21], v203 offset:49152
	ds_read_b128 v[22:25], v203 offset:50176
	ds_read_b128 v[26:29], v203 offset:51200
	ds_read_b128 v[30:33], v203 offset:52224
	ds_read_b128 v[210:213], v203 offset:53248
	ds_read_b128 v[214:217], v203 offset:54272
	ds_read_b128 v[218:221], v203 offset:55296
	ds_read_b128 v[222:225], v203 offset:56320
	global_load_lds_dwordx4 v[188:189], off
	v_lshl_add_u64 v[188:189], v[192:193], 0, s[16:17]
	s_mov_b32 m0, s38
	s_nop 0
	global_load_lds_dwordx4 v[188:189], off
	s_waitcnt vmcnt(10)
	s_barrier
	s_waitcnt lgkmcnt(0)
	s_waitcnt lgkmcnt(0)
	v_mfma_f32_16x16x128_f8f6f4 v[94:97], v[2:9], v[18:25], v[94:97]
	v_mfma_f32_16x16x128_f8f6f4 v[86:89], v[10:17], v[18:25], v[86:89]
	v_mfma_f32_16x16x128_f8f6f4 v[78:81], v[2:9], v[26:33], v[78:81]
	v_mfma_f32_16x16x128_f8f6f4 v[70:73], v[10:17], v[26:33], v[70:73]
	v_mfma_f32_16x16x128_f8f6f4 v[62:65], v[2:9], v[210:217], v[62:65]
	v_mfma_f32_16x16x128_f8f6f4 v[54:57], v[10:17], v[210:217], v[54:57]
	v_mfma_f32_16x16x128_f8f6f4 v[46:49], v[2:9], v[218:225], v[46:49]
	v_mfma_f32_16x16x128_f8f6f4 v[38:41], v[10:17], v[218:225], v[38:41]
	s_barrier
	v_add_u32_e32 v14, s39, v201
	ds_read_b128 v[2:5], v14
	ds_read_b128 v[6:9], v14 offset:1024
	ds_read_b128 v[10:13], v14 offset:2048
	ds_read_b128 v[14:17], v14 offset:3072
	s_add_u32 s24, s24, 0x40080
	s_addc_u32 s25, s25, 0
	s_add_i32 s26, s26, s23
	v_lshl_add_u64 v[242:243], s[24:25], 0, v[164:165]
	s_mov_b32 m0, s26
	s_nop 0
	global_load_lds_dwordx4 v[242:243], off
	v_lshl_add_u64 v[242:243], s[24:25], 0, v[166:167]
	s_add_i32 m0, s26, 0x2000
	s_nop 0
	global_load_lds_dwordx4 v[242:243], off
	s_waitcnt vmcnt(6)
	s_barrier
	v_mfma_f32_16x16x128_f8f6f4 v[90:93], v[226:233], v[18:25], v[90:93]
	v_mfma_f32_16x16x128_f8f6f4 v[82:85], v[234:241], v[18:25], v[82:85]
	v_mfma_f32_16x16x128_f8f6f4 v[74:77], v[226:233], v[26:33], v[74:77]
	v_mfma_f32_16x16x128_f8f6f4 v[66:69], v[234:241], v[26:33], v[66:69]
	v_mfma_f32_16x16x128_f8f6f4 v[58:61], v[226:233], v[210:217], v[58:61]
	v_mfma_f32_16x16x128_f8f6f4 v[50:53], v[234:241], v[210:217], v[50:53]
	v_mfma_f32_16x16x128_f8f6f4 v[42:45], v[226:233], v[218:225], v[42:45]
	v_mfma_f32_16x16x128_f8f6f4 v[34:37], v[234:241], v[218:225], v[34:37]
	s_add_i32 s52, s52, 2
	s_cmp_gt_u32 s52, 13
	s_mov_b64 s[26:27], s[4:5]
	s_barrier
	s_cbranch_scc0 .LBB0_1060
	s_waitcnt lgkmcnt(0)
	v_lshl_add_u32 v4, s48, 8, v179
	s_lshl_b32 s4, s22, 7
	v_ashrrev_i32_e32 v5, 31, v4
	s_and_b32 s4, s4, 0x780
	v_lshlrev_b64 v[2:3], 11, v[4:5]
	v_or_b32_e32 v162, s4, v202
	v_lshl_add_u64 v[2:3], s[12:13], 0, v[2:3]
	v_lshl_add_u64 v[2:3], v[2:3], 0, v[162:163]
	s_nop 15
	s_nop 15
	v_mul_f32_e32 v6, 0xbcb8aa3b, v158
	v_mul_f32_e32 v7, 0xbcb8aa3b, v159
	v_mul_f32_e32 v8, 0xbcb8aa3b, v160
	v_mul_f32_e32 v9, 0xbcb8aa3b, v161
	v_mul_f32_e32 v10, 0xbcb8aa3b, v150
	v_mul_f32_e32 v11, 0xbcb8aa3b, v151
	v_mul_f32_e32 v12, 0xbcb8aa3b, v152
	v_mul_f32_e32 v13, 0xbcb8aa3b, v153
	v_exp_f32_e32 v6, v6
	v_exp_f32_e32 v7, v7
	v_exp_f32_e32 v8, v8
	v_exp_f32_e32 v9, v9
	v_exp_f32_e32 v10, v10
	v_exp_f32_e32 v11, v11
	v_exp_f32_e32 v12, v12
	v_exp_f32_e32 v13, v13
	v_mul_f32_e32 v158, v158, v154
	v_mul_f32_e32 v159, v159, v155
	v_mul_f32_e32 v160, v160, v156
	v_mul_f32_e32 v161, v161, v157
	v_mul_f32_e32 v150, v150, v146
	v_mul_f32_e32 v151, v151, v147
	v_mul_f32_e32 v152, v152, v148
	v_mul_f32_e32 v153, v153, v149
	v_add_f32_e32 v6, 1.0, v6
	v_add_f32_e32 v7, 1.0, v7
	v_add_f32_e32 v8, 1.0, v8
	v_add_f32_e32 v9, 1.0, v9
	v_add_f32_e32 v10, 1.0, v10
	v_add_f32_e32 v11, 1.0, v11
	v_add_f32_e32 v12, 1.0, v12
	v_add_f32_e32 v13, 1.0, v13
	v_rcp_f32_e32 v6, v6
	v_rcp_f32_e32 v7, v7
	v_rcp_f32_e32 v8, v8
	v_rcp_f32_e32 v9, v9
	v_rcp_f32_e32 v10, v10
	v_rcp_f32_e32 v11, v11
	v_rcp_f32_e32 v12, v12
	v_rcp_f32_e32 v13, v13
	v_mul_f32_e32 v158, v6, v158
	v_mul_f32_e32 v159, v7, v159
	v_mul_f32_e32 v160, v8, v160
	v_mul_f32_e32 v161, v9, v161
	v_mul_f32_e32 v150, v10, v150
	v_mul_f32_e32 v151, v11, v151
	v_mul_f32_e32 v152, v12, v152
	v_mul_f32_e32 v153, v13, v153
	v_mul_f32_e32 v158, 0x3a800000, v158
	v_mul_f32_e32 v159, 0x3a800000, v159
	v_mul_f32_e32 v160, 0x3a800000, v160
	v_mul_f32_e32 v161, 0x3a800000, v161
	v_mul_f32_e32 v150, 0x3a800000, v150
	v_mul_f32_e32 v151, 0x3a800000, v151
	v_mul_f32_e32 v152, 0x3a800000, v152
	v_mul_f32_e32 v153, 0x3a800000, v153
	v_med3_f32 v158, v158, s41, v205
	v_med3_f32 v159, v159, s41, v205
	v_med3_f32 v160, v160, s41, v205
	v_med3_f32 v161, v161, s41, v205
	v_med3_f32 v150, v150, s41, v205
	v_med3_f32 v151, v151, s41, v205
	v_med3_f32 v152, v152, s41, v205
	v_med3_f32 v153, v153, s41, v205
	v_cvt_pk_fp8_f32 v14, v158, v159
	v_cvt_pk_fp8_f32 v15, v150, v151
	v_cvt_pk_fp8_f32 v14, v160, v161 op_sel:[0,0,1]
	v_cvt_pk_fp8_f32 v15, v152, v153 op_sel:[0,0,1]
	s_nop 0
	global_store_dwordx2 v[2:3], v[14:15], off
	v_mul_f32_e32 v6, 0xbcb8aa3b, v142
	v_mul_f32_e32 v7, 0xbcb8aa3b, v143
	v_mul_f32_e32 v8, 0xbcb8aa3b, v144
	v_mul_f32_e32 v9, 0xbcb8aa3b, v145
	v_mul_f32_e32 v10, 0xbcb8aa3b, v134
	v_mul_f32_e32 v11, 0xbcb8aa3b, v135
	v_mul_f32_e32 v12, 0xbcb8aa3b, v136
	v_mul_f32_e32 v13, 0xbcb8aa3b, v137
	v_exp_f32_e32 v6, v6
	v_exp_f32_e32 v7, v7
	v_exp_f32_e32 v8, v8
	v_exp_f32_e32 v9, v9
	v_exp_f32_e32 v10, v10
	v_exp_f32_e32 v11, v11
	v_exp_f32_e32 v12, v12
	v_exp_f32_e32 v13, v13
	v_mul_f32_e32 v142, v142, v138
	v_mul_f32_e32 v143, v143, v139
	v_mul_f32_e32 v144, v144, v140
	v_mul_f32_e32 v145, v145, v141
	v_mul_f32_e32 v134, v134, v130
	v_mul_f32_e32 v135, v135, v131
	v_mul_f32_e32 v136, v136, v132
	v_mul_f32_e32 v137, v137, v133
	v_add_f32_e32 v6, 1.0, v6
	v_add_f32_e32 v7, 1.0, v7
	v_add_f32_e32 v8, 1.0, v8
	v_add_f32_e32 v9, 1.0, v9
	v_add_f32_e32 v10, 1.0, v10
	v_add_f32_e32 v11, 1.0, v11
	v_add_f32_e32 v12, 1.0, v12
	v_add_f32_e32 v13, 1.0, v13
	v_rcp_f32_e32 v6, v6
	v_rcp_f32_e32 v7, v7
	v_rcp_f32_e32 v8, v8
	v_rcp_f32_e32 v9, v9
	v_rcp_f32_e32 v10, v10
	v_rcp_f32_e32 v11, v11
	v_rcp_f32_e32 v12, v12
	v_rcp_f32_e32 v13, v13
	v_add_co_u32_e32 v4, vcc, 0x8000, v2
	v_mul_f32_e32 v142, v6, v142
	v_mul_f32_e32 v143, v7, v143
	v_mul_f32_e32 v144, v8, v144
	v_mul_f32_e32 v145, v9, v145
	v_mul_f32_e32 v134, v10, v134
	v_mul_f32_e32 v135, v11, v135
	v_mul_f32_e32 v136, v12, v136
	v_mul_f32_e32 v137, v13, v137
	v_addc_co_u32_e32 v5, vcc, 0, v3, vcc
	v_mul_f32_e32 v142, 0x3a800000, v142
	v_mul_f32_e32 v143, 0x3a800000, v143
	v_mul_f32_e32 v144, 0x3a800000, v144
	v_mul_f32_e32 v145, 0x3a800000, v145
	v_mul_f32_e32 v134, 0x3a800000, v134
	v_mul_f32_e32 v135, 0x3a800000, v135
	v_mul_f32_e32 v136, 0x3a800000, v136
	v_mul_f32_e32 v137, 0x3a800000, v137
	v_med3_f32 v142, v142, s41, v205
	v_med3_f32 v143, v143, s41, v205
	v_med3_f32 v144, v144, s41, v205
	v_med3_f32 v145, v145, s41, v205
	v_med3_f32 v134, v134, s41, v205
	v_med3_f32 v135, v135, s41, v205
	v_med3_f32 v136, v136, s41, v205
	v_med3_f32 v137, v137, s41, v205
	v_cvt_pk_fp8_f32 v16, v142, v143
	v_cvt_pk_fp8_f32 v17, v134, v135
	v_cvt_pk_fp8_f32 v16, v144, v145 op_sel:[0,0,1]
	v_cvt_pk_fp8_f32 v17, v136, v137 op_sel:[0,0,1]
	s_nop 0
	global_store_dwordx2 v[4:5], v[16:17], off
	v_mul_f32_e32 v6, 0xbcb8aa3b, v126
	v_mul_f32_e32 v7, 0xbcb8aa3b, v127
	v_mul_f32_e32 v8, 0xbcb8aa3b, v128
	v_mul_f32_e32 v9, 0xbcb8aa3b, v129
	v_mul_f32_e32 v10, 0xbcb8aa3b, v118
	v_mul_f32_e32 v11, 0xbcb8aa3b, v119
	v_mul_f32_e32 v12, 0xbcb8aa3b, v120
	v_mul_f32_e32 v13, 0xbcb8aa3b, v121
	v_exp_f32_e32 v6, v6
	v_exp_f32_e32 v7, v7
	v_exp_f32_e32 v8, v8
	v_exp_f32_e32 v9, v9
	v_exp_f32_e32 v10, v10
	v_exp_f32_e32 v11, v11
	v_exp_f32_e32 v12, v12
	v_exp_f32_e32 v13, v13
	v_mul_f32_e32 v126, v126, v122
	v_mul_f32_e32 v127, v127, v123
	v_mul_f32_e32 v128, v128, v124
	v_mul_f32_e32 v129, v129, v125
	v_mul_f32_e32 v118, v118, v114
	v_mul_f32_e32 v119, v119, v115
	v_mul_f32_e32 v120, v120, v116
	v_mul_f32_e32 v121, v121, v117
	v_add_f32_e32 v6, 1.0, v6
	v_add_f32_e32 v7, 1.0, v7
	v_add_f32_e32 v8, 1.0, v8
	v_add_f32_e32 v9, 1.0, v9
	v_add_f32_e32 v10, 1.0, v10
	v_add_f32_e32 v11, 1.0, v11
	v_add_f32_e32 v12, 1.0, v12
	v_add_f32_e32 v13, 1.0, v13
	v_rcp_f32_e32 v6, v6
	v_rcp_f32_e32 v7, v7
	v_rcp_f32_e32 v8, v8
	v_rcp_f32_e32 v9, v9
	v_rcp_f32_e32 v10, v10
	v_rcp_f32_e32 v11, v11
	v_rcp_f32_e32 v12, v12
	v_rcp_f32_e32 v13, v13
	v_add_co_u32_e32 v4, vcc, 0x10000, v2
	v_mul_f32_e32 v126, v6, v126
	v_mul_f32_e32 v127, v7, v127
	v_mul_f32_e32 v128, v8, v128
	v_mul_f32_e32 v129, v9, v129
	v_mul_f32_e32 v118, v10, v118
	v_mul_f32_e32 v119, v11, v119
	v_mul_f32_e32 v120, v12, v120
	v_mul_f32_e32 v121, v13, v121
	v_addc_co_u32_e32 v5, vcc, 0, v3, vcc
	v_mul_f32_e32 v126, 0x3a800000, v126
	v_mul_f32_e32 v127, 0x3a800000, v127
	v_mul_f32_e32 v128, 0x3a800000, v128
	v_mul_f32_e32 v129, 0x3a800000, v129
	v_mul_f32_e32 v118, 0x3a800000, v118
	v_mul_f32_e32 v119, 0x3a800000, v119
	v_mul_f32_e32 v120, 0x3a800000, v120
	v_mul_f32_e32 v121, 0x3a800000, v121
	v_med3_f32 v126, v126, s41, v205
	v_med3_f32 v127, v127, s41, v205
	v_med3_f32 v128, v128, s41, v205
	v_med3_f32 v129, v129, s41, v205
	v_med3_f32 v118, v118, s41, v205
	v_med3_f32 v119, v119, s41, v205
	v_med3_f32 v120, v120, s41, v205
	v_med3_f32 v121, v121, s41, v205
	v_cvt_pk_fp8_f32 v14, v126, v127
	v_cvt_pk_fp8_f32 v15, v118, v119
	v_cvt_pk_fp8_f32 v14, v128, v129 op_sel:[0,0,1]
	v_cvt_pk_fp8_f32 v15, v120, v121 op_sel:[0,0,1]
	s_nop 0
	global_store_dwordx2 v[4:5], v[14:15], off
	v_mul_f32_e32 v6, 0xbcb8aa3b, v110
	v_mul_f32_e32 v7, 0xbcb8aa3b, v111
	v_mul_f32_e32 v8, 0xbcb8aa3b, v112
	v_mul_f32_e32 v9, 0xbcb8aa3b, v113
	v_mul_f32_e32 v10, 0xbcb8aa3b, v102
	v_mul_f32_e32 v11, 0xbcb8aa3b, v103
	v_mul_f32_e32 v12, 0xbcb8aa3b, v104
	v_mul_f32_e32 v13, 0xbcb8aa3b, v105
	v_exp_f32_e32 v6, v6
	v_exp_f32_e32 v7, v7
	v_exp_f32_e32 v8, v8
	v_exp_f32_e32 v9, v9
	v_exp_f32_e32 v10, v10
	v_exp_f32_e32 v11, v11
	v_exp_f32_e32 v12, v12
	v_exp_f32_e32 v13, v13
	v_mul_f32_e32 v110, v110, v106
	v_mul_f32_e32 v111, v111, v107
	v_mul_f32_e32 v112, v112, v108
	v_mul_f32_e32 v113, v113, v109
	v_mul_f32_e32 v102, v102, v98
	v_mul_f32_e32 v103, v103, v99
	v_mul_f32_e32 v104, v104, v100
	v_mul_f32_e32 v105, v105, v101
	v_add_f32_e32 v6, 1.0, v6
	v_add_f32_e32 v7, 1.0, v7
	v_add_f32_e32 v8, 1.0, v8
	v_add_f32_e32 v9, 1.0, v9
	v_add_f32_e32 v10, 1.0, v10
	v_add_f32_e32 v11, 1.0, v11
	v_add_f32_e32 v12, 1.0, v12
	v_add_f32_e32 v13, 1.0, v13
	v_rcp_f32_e32 v6, v6
	v_rcp_f32_e32 v7, v7
	v_rcp_f32_e32 v8, v8
	v_rcp_f32_e32 v9, v9
	v_rcp_f32_e32 v10, v10
	v_rcp_f32_e32 v11, v11
	v_rcp_f32_e32 v12, v12
	v_rcp_f32_e32 v13, v13
	v_add_co_u32_e32 v4, vcc, 0x18000, v2
	v_mul_f32_e32 v110, v6, v110
	v_mul_f32_e32 v111, v7, v111
	v_mul_f32_e32 v112, v8, v112
	v_mul_f32_e32 v113, v9, v113
	v_mul_f32_e32 v102, v10, v102
	v_mul_f32_e32 v103, v11, v103
	v_mul_f32_e32 v104, v12, v104
	v_mul_f32_e32 v105, v13, v105
	v_addc_co_u32_e32 v5, vcc, 0, v3, vcc
	v_mul_f32_e32 v110, 0x3a800000, v110
	v_mul_f32_e32 v111, 0x3a800000, v111
	v_mul_f32_e32 v112, 0x3a800000, v112
	v_mul_f32_e32 v113, 0x3a800000, v113
	v_mul_f32_e32 v102, 0x3a800000, v102
	v_mul_f32_e32 v103, 0x3a800000, v103
	v_mul_f32_e32 v104, 0x3a800000, v104
	v_mul_f32_e32 v105, 0x3a800000, v105
	v_med3_f32 v110, v110, s41, v205
	v_med3_f32 v111, v111, s41, v205
	v_med3_f32 v112, v112, s41, v205
	v_med3_f32 v113, v113, s41, v205
	v_med3_f32 v102, v102, s41, v205
	v_med3_f32 v103, v103, s41, v205
	v_med3_f32 v104, v104, s41, v205
	v_med3_f32 v105, v105, s41, v205
	v_cvt_pk_fp8_f32 v16, v110, v111
	v_cvt_pk_fp8_f32 v17, v102, v103
	v_cvt_pk_fp8_f32 v16, v112, v113 op_sel:[0,0,1]
	v_cvt_pk_fp8_f32 v17, v104, v105 op_sel:[0,0,1]
	s_nop 0
	global_store_dwordx2 v[4:5], v[16:17], off
	v_mul_f32_e32 v6, 0xbcb8aa3b, v94
	v_mul_f32_e32 v7, 0xbcb8aa3b, v95
	v_mul_f32_e32 v8, 0xbcb8aa3b, v96
	v_mul_f32_e32 v9, 0xbcb8aa3b, v97
	v_mul_f32_e32 v10, 0xbcb8aa3b, v86
	v_mul_f32_e32 v11, 0xbcb8aa3b, v87
	v_mul_f32_e32 v12, 0xbcb8aa3b, v88
	v_mul_f32_e32 v13, 0xbcb8aa3b, v89
	v_exp_f32_e32 v6, v6
	v_exp_f32_e32 v7, v7
	v_exp_f32_e32 v8, v8
	v_exp_f32_e32 v9, v9
	v_exp_f32_e32 v10, v10
	v_exp_f32_e32 v11, v11
	v_exp_f32_e32 v12, v12
	v_exp_f32_e32 v13, v13
	v_mul_f32_e32 v94, v94, v90
	v_mul_f32_e32 v95, v95, v91
	v_mul_f32_e32 v96, v96, v92
	v_mul_f32_e32 v97, v97, v93
	v_mul_f32_e32 v86, v86, v82
	v_mul_f32_e32 v87, v87, v83
	v_mul_f32_e32 v88, v88, v84
	v_mul_f32_e32 v89, v89, v85
	v_add_f32_e32 v6, 1.0, v6
	v_add_f32_e32 v7, 1.0, v7
	v_add_f32_e32 v8, 1.0, v8
	v_add_f32_e32 v9, 1.0, v9
	v_add_f32_e32 v10, 1.0, v10
	v_add_f32_e32 v11, 1.0, v11
	v_add_f32_e32 v12, 1.0, v12
	v_add_f32_e32 v13, 1.0, v13
	v_rcp_f32_e32 v6, v6
	v_rcp_f32_e32 v7, v7
	v_rcp_f32_e32 v8, v8
	v_rcp_f32_e32 v9, v9
	v_rcp_f32_e32 v10, v10
	v_rcp_f32_e32 v11, v11
	v_rcp_f32_e32 v12, v12
	v_rcp_f32_e32 v13, v13
	v_add_co_u32_e32 v4, vcc, 0x40000, v2
	v_mul_f32_e32 v94, v6, v94
	v_mul_f32_e32 v95, v7, v95
	v_mul_f32_e32 v96, v8, v96
	v_mul_f32_e32 v97, v9, v97
	v_mul_f32_e32 v86, v10, v86
	v_mul_f32_e32 v87, v11, v87
	v_mul_f32_e32 v88, v12, v88
	v_mul_f32_e32 v89, v13, v89
	v_addc_co_u32_e32 v5, vcc, 0, v3, vcc
	v_mul_f32_e32 v94, 0x3a800000, v94
	v_mul_f32_e32 v95, 0x3a800000, v95
	v_mul_f32_e32 v96, 0x3a800000, v96
	v_mul_f32_e32 v97, 0x3a800000, v97
	v_mul_f32_e32 v86, 0x3a800000, v86
	v_mul_f32_e32 v87, 0x3a800000, v87
	v_mul_f32_e32 v88, 0x3a800000, v88
	v_mul_f32_e32 v89, 0x3a800000, v89
	v_med3_f32 v94, v94, s41, v205
	v_med3_f32 v95, v95, s41, v205
	v_med3_f32 v96, v96, s41, v205
	v_med3_f32 v97, v97, s41, v205
	v_med3_f32 v86, v86, s41, v205
	v_med3_f32 v87, v87, s41, v205
	v_med3_f32 v88, v88, s41, v205
	v_med3_f32 v89, v89, s41, v205
	v_cvt_pk_fp8_f32 v14, v94, v95
	v_cvt_pk_fp8_f32 v15, v86, v87
	v_cvt_pk_fp8_f32 v14, v96, v97 op_sel:[0,0,1]
	v_cvt_pk_fp8_f32 v15, v88, v89 op_sel:[0,0,1]
	s_nop 0
	global_store_dwordx2 v[4:5], v[14:15], off
	v_mul_f32_e32 v6, 0xbcb8aa3b, v78
	v_mul_f32_e32 v7, 0xbcb8aa3b, v79
	v_mul_f32_e32 v8, 0xbcb8aa3b, v80
	v_mul_f32_e32 v9, 0xbcb8aa3b, v81
	v_mul_f32_e32 v10, 0xbcb8aa3b, v70
	v_mul_f32_e32 v11, 0xbcb8aa3b, v71
	v_mul_f32_e32 v12, 0xbcb8aa3b, v72
	v_mul_f32_e32 v13, 0xbcb8aa3b, v73
	v_exp_f32_e32 v6, v6
	v_exp_f32_e32 v7, v7
	v_exp_f32_e32 v8, v8
	v_exp_f32_e32 v9, v9
	v_exp_f32_e32 v10, v10
	v_exp_f32_e32 v11, v11
	v_exp_f32_e32 v12, v12
	v_exp_f32_e32 v13, v13
	v_mul_f32_e32 v78, v78, v74
	v_mul_f32_e32 v79, v79, v75
	v_mul_f32_e32 v80, v80, v76
	v_mul_f32_e32 v81, v81, v77
	v_mul_f32_e32 v70, v70, v66
	v_mul_f32_e32 v71, v71, v67
	v_mul_f32_e32 v72, v72, v68
	v_mul_f32_e32 v73, v73, v69
	v_add_f32_e32 v6, 1.0, v6
	v_add_f32_e32 v7, 1.0, v7
	v_add_f32_e32 v8, 1.0, v8
	v_add_f32_e32 v9, 1.0, v9
	v_add_f32_e32 v10, 1.0, v10
	v_add_f32_e32 v11, 1.0, v11
	v_add_f32_e32 v12, 1.0, v12
	v_add_f32_e32 v13, 1.0, v13
	v_rcp_f32_e32 v6, v6
	v_rcp_f32_e32 v7, v7
	v_rcp_f32_e32 v8, v8
	v_rcp_f32_e32 v9, v9
	v_rcp_f32_e32 v10, v10
	v_rcp_f32_e32 v11, v11
	v_rcp_f32_e32 v12, v12
	v_rcp_f32_e32 v13, v13
	v_add_co_u32_e32 v4, vcc, 0x48000, v2
	v_mul_f32_e32 v78, v6, v78
	v_mul_f32_e32 v79, v7, v79
	v_mul_f32_e32 v80, v8, v80
	v_mul_f32_e32 v81, v9, v81
	v_mul_f32_e32 v70, v10, v70
	v_mul_f32_e32 v71, v11, v71
	v_mul_f32_e32 v72, v12, v72
	v_mul_f32_e32 v73, v13, v73
	v_addc_co_u32_e32 v5, vcc, 0, v3, vcc
	v_mul_f32_e32 v78, 0x3a800000, v78
	v_mul_f32_e32 v79, 0x3a800000, v79
	v_mul_f32_e32 v80, 0x3a800000, v80
	v_mul_f32_e32 v81, 0x3a800000, v81
	v_mul_f32_e32 v70, 0x3a800000, v70
	v_mul_f32_e32 v71, 0x3a800000, v71
	v_mul_f32_e32 v72, 0x3a800000, v72
	v_mul_f32_e32 v73, 0x3a800000, v73
	v_med3_f32 v78, v78, s41, v205
	v_med3_f32 v79, v79, s41, v205
	v_med3_f32 v80, v80, s41, v205
	v_med3_f32 v81, v81, s41, v205
	v_med3_f32 v70, v70, s41, v205
	v_med3_f32 v71, v71, s41, v205
	v_med3_f32 v72, v72, s41, v205
	v_med3_f32 v73, v73, s41, v205
	v_cvt_pk_fp8_f32 v16, v78, v79
	v_cvt_pk_fp8_f32 v17, v70, v71
	v_cvt_pk_fp8_f32 v16, v80, v81 op_sel:[0,0,1]
	v_cvt_pk_fp8_f32 v17, v72, v73 op_sel:[0,0,1]
	s_nop 0
	global_store_dwordx2 v[4:5], v[16:17], off
	v_mul_f32_e32 v6, 0xbcb8aa3b, v62
	v_mul_f32_e32 v7, 0xbcb8aa3b, v63
	v_mul_f32_e32 v8, 0xbcb8aa3b, v64
	v_mul_f32_e32 v9, 0xbcb8aa3b, v65
	v_mul_f32_e32 v10, 0xbcb8aa3b, v54
	v_mul_f32_e32 v11, 0xbcb8aa3b, v55
	v_mul_f32_e32 v12, 0xbcb8aa3b, v56
	v_mul_f32_e32 v13, 0xbcb8aa3b, v57
	v_exp_f32_e32 v6, v6
	v_exp_f32_e32 v7, v7
	v_exp_f32_e32 v8, v8
	v_exp_f32_e32 v9, v9
	v_exp_f32_e32 v10, v10
	v_exp_f32_e32 v11, v11
	v_exp_f32_e32 v12, v12
	v_exp_f32_e32 v13, v13
	v_mul_f32_e32 v62, v62, v58
	v_mul_f32_e32 v63, v63, v59
	v_mul_f32_e32 v64, v64, v60
	v_mul_f32_e32 v65, v65, v61
	v_mul_f32_e32 v54, v54, v50
	v_mul_f32_e32 v55, v55, v51
	v_mul_f32_e32 v56, v56, v52
	v_mul_f32_e32 v57, v57, v53
	v_add_f32_e32 v6, 1.0, v6
	v_add_f32_e32 v7, 1.0, v7
	v_add_f32_e32 v8, 1.0, v8
	v_add_f32_e32 v9, 1.0, v9
	v_add_f32_e32 v10, 1.0, v10
	v_add_f32_e32 v11, 1.0, v11
	v_add_f32_e32 v12, 1.0, v12
	v_add_f32_e32 v13, 1.0, v13
	v_rcp_f32_e32 v6, v6
	v_rcp_f32_e32 v7, v7
	v_rcp_f32_e32 v8, v8
	v_rcp_f32_e32 v9, v9
	v_rcp_f32_e32 v10, v10
	v_rcp_f32_e32 v11, v11
	v_rcp_f32_e32 v12, v12
	v_rcp_f32_e32 v13, v13
	v_add_co_u32_e32 v4, vcc, 0x50000, v2
	v_mul_f32_e32 v62, v6, v62
	v_mul_f32_e32 v63, v7, v63
	v_mul_f32_e32 v64, v8, v64
	v_mul_f32_e32 v65, v9, v65
	v_mul_f32_e32 v54, v10, v54
	v_mul_f32_e32 v55, v11, v55
	v_mul_f32_e32 v56, v12, v56
	v_mul_f32_e32 v57, v13, v57
	v_addc_co_u32_e32 v5, vcc, 0, v3, vcc
	v_mul_f32_e32 v62, 0x3a800000, v62
	v_mul_f32_e32 v63, 0x3a800000, v63
	v_mul_f32_e32 v64, 0x3a800000, v64
	v_mul_f32_e32 v65, 0x3a800000, v65
	v_mul_f32_e32 v54, 0x3a800000, v54
	v_mul_f32_e32 v55, 0x3a800000, v55
	v_mul_f32_e32 v56, 0x3a800000, v56
	v_mul_f32_e32 v57, 0x3a800000, v57
	v_med3_f32 v62, v62, s41, v205
	v_med3_f32 v63, v63, s41, v205
	v_med3_f32 v64, v64, s41, v205
	v_med3_f32 v65, v65, s41, v205
	v_med3_f32 v54, v54, s41, v205
	v_med3_f32 v55, v55, s41, v205
	v_med3_f32 v56, v56, s41, v205
	v_med3_f32 v57, v57, s41, v205
	v_cvt_pk_fp8_f32 v14, v62, v63
	v_cvt_pk_fp8_f32 v15, v54, v55
	v_cvt_pk_fp8_f32 v14, v64, v65 op_sel:[0,0,1]
	v_cvt_pk_fp8_f32 v15, v56, v57 op_sel:[0,0,1]
	s_nop 0
	global_store_dwordx2 v[4:5], v[14:15], off
	v_mul_f32_e32 v6, 0xbcb8aa3b, v46
	v_mul_f32_e32 v7, 0xbcb8aa3b, v47
	v_mul_f32_e32 v8, 0xbcb8aa3b, v48
	v_mul_f32_e32 v9, 0xbcb8aa3b, v49
	v_mul_f32_e32 v10, 0xbcb8aa3b, v38
	v_mul_f32_e32 v11, 0xbcb8aa3b, v39
	v_mul_f32_e32 v12, 0xbcb8aa3b, v40
	v_mul_f32_e32 v13, 0xbcb8aa3b, v41
	v_exp_f32_e32 v6, v6
	v_exp_f32_e32 v7, v7
	v_exp_f32_e32 v8, v8
	v_exp_f32_e32 v9, v9
	v_exp_f32_e32 v10, v10
	v_exp_f32_e32 v11, v11
	v_exp_f32_e32 v12, v12
	v_exp_f32_e32 v13, v13
	v_mul_f32_e32 v46, v46, v42
	v_mul_f32_e32 v47, v47, v43
	v_mul_f32_e32 v48, v48, v44
	v_mul_f32_e32 v49, v49, v45
	v_mul_f32_e32 v38, v38, v34
	v_mul_f32_e32 v39, v39, v35
	v_mul_f32_e32 v40, v40, v36
	v_mul_f32_e32 v41, v41, v37
	v_add_f32_e32 v6, 1.0, v6
	v_add_f32_e32 v7, 1.0, v7
	v_add_f32_e32 v8, 1.0, v8
	v_add_f32_e32 v9, 1.0, v9
	v_add_f32_e32 v10, 1.0, v10
	v_add_f32_e32 v11, 1.0, v11
	v_add_f32_e32 v12, 1.0, v12
	v_add_f32_e32 v13, 1.0, v13
	v_rcp_f32_e32 v6, v6
	v_rcp_f32_e32 v7, v7
	v_rcp_f32_e32 v8, v8
	v_rcp_f32_e32 v9, v9
	v_rcp_f32_e32 v10, v10
	v_rcp_f32_e32 v11, v11
	v_rcp_f32_e32 v12, v12
	v_rcp_f32_e32 v13, v13
	v_add_co_u32_e32 v4, vcc, 0x58000, v2
	v_mul_f32_e32 v46, v6, v46
	v_mul_f32_e32 v47, v7, v47
	v_mul_f32_e32 v48, v8, v48
	v_mul_f32_e32 v49, v9, v49
	v_mul_f32_e32 v38, v10, v38
	v_mul_f32_e32 v39, v11, v39
	v_mul_f32_e32 v40, v12, v40
	v_mul_f32_e32 v41, v13, v41
	v_addc_co_u32_e32 v5, vcc, 0, v3, vcc
	v_mul_f32_e32 v46, 0x3a800000, v46
	v_mul_f32_e32 v47, 0x3a800000, v47
	v_mul_f32_e32 v48, 0x3a800000, v48
	v_mul_f32_e32 v49, 0x3a800000, v49
	v_mul_f32_e32 v38, 0x3a800000, v38
	v_mul_f32_e32 v39, 0x3a800000, v39
	v_mul_f32_e32 v40, 0x3a800000, v40
	v_mul_f32_e32 v41, 0x3a800000, v41
	v_med3_f32 v46, v46, s41, v205
	v_med3_f32 v47, v47, s41, v205
	v_med3_f32 v48, v48, s41, v205
	v_med3_f32 v49, v49, s41, v205
	v_med3_f32 v38, v38, s41, v205
	v_med3_f32 v39, v39, s41, v205
	v_med3_f32 v40, v40, s41, v205
	v_med3_f32 v41, v41, s41, v205
	v_cvt_pk_fp8_f32 v16, v46, v47
	v_cvt_pk_fp8_f32 v17, v38, v39
	v_cvt_pk_fp8_f32 v16, v48, v49 op_sel:[0,0,1]
	v_cvt_pk_fp8_f32 v17, v40, v41 op_sel:[0,0,1]
	v_mov_b32_e32 v182, v176
	v_mov_b32_e32 v180, v174
	v_mov_b32_e32 v178, v207
	v_mov_b32_e32 v208, v206
	s_and_b64 vcc, exec, s[0:1]
	s_mov_b32 s48, s47
	s_mov_b32 s22, s20
	s_mov_b64 s[24:25], s[6:7]
	s_mov_b32 s21, s45
	global_store_dwordx2 v[4:5], v[16:17], off
	s_cbranch_vccz .LBB0_1042
	s_waitcnt vmcnt(0)
	s_cmpk_gt_u32 s19, 0xff
	s_cbranch_scc1 .LBB0_1064
	s_barrier
